# phase 8 router-logit loop: 16 operand loads per iteration in flight with counted waits; on top of v36
# speedup vs baseline: 1.0051x; 1.0038x over previous
; #define GAS __attribute__((address_space(1)))
; #define LAS __attribute__((address_space(3)))
; __device__ __forceinline__ void phase8(KP kp, LAS unsigned char* lds, int wave, int bid) {
;     ...
;     {
;         const int i = lane & 31, hk = lane >> 5; const float rstd_i = rs[i];
;         const float* xrow = X1 + (size_t)(32 * bid + i) * DM + 256 * wave + 16 * hk; const float* wrow = wrt + (size_t)i * DM + 256 * wave + 16 * hk;
;         const LAS float* a2p = A2 + 256 * wave + 16 * hk; const LAS float* b2p = B2 + 256 * wave + 16 * hk;
;         f32x16 acc = {0.f, 0.f, 0.f, 0.f, 0.f, 0.f, 0.f, 0.f, 0.f, 0.f, 0.f, 0.f, 0.f, 0.f, 0.f, 0.f};
; #pragma unroll 2
;         for (int kb = 0; kb < 8; ++kb) {
;             f32x4 xv[4], wv[4];
; #pragma unroll
;             for (int q = 0; q < 4; ++q) { xv[q] = *(const GAS f32x4*)(xrow + 32 * kb + 4 * q); wv[q] = *(const GAS f32x4*)(wrow + 32 * kb + 4 * q); }
; #pragma unroll
;             for (int q = 0; q < 4; ++q) { const f32x4 av = *(const LAS f32x4*)(a2p + 32 * kb + 4 * q), bv = *(const LAS f32x4*)(b2p + 32 * kb + 4 * q); xv[q] = xv[q] * rstd_i * av + bv; }
; #pragma unroll
;             for (int q = 0; q < 4; ++q) {
;                 acc = __builtin_amdgcn_mfma_f32_32x32x2f32(xv[q].x, wv[q].x, acc, 0, 0, 0); acc = __builtin_amdgcn_mfma_f32_32x32x2f32(xv[q].y, wv[q].y, acc, 0, 0, 0);
;                 acc = __builtin_amdgcn_mfma_f32_32x32x2f32(xv[q].z, wv[q].z, acc, 0, 0, 0); acc = __builtin_amdgcn_mfma_f32_32x32x2f32(xv[q].w, wv[q].w, acc, 0, 0, 0); }
;         }
; #pragma unroll
;         for (int r = 0; r < 16; ++r) part[(wave * 32 + (r & 3) + 8 * (r >> 2) + 4 * hk) * 33 + i] = acc[r];
;     }
;     __syncthreads();
.LBB0_938:
	v_lshl_add_u64 v[62:63], v[22:23], 0, s[2:3]
	v_lshl_add_u64 v[64:65], v[24:25], 0, s[2:3]
	global_load_dwordx4 v[66:69], v[62:63], off offset:-128
	global_load_dwordx4 v[98:101], v[64:65], off offset:-128
	global_load_dwordx4 v[70:73], v[62:63], off offset:-112
	global_load_dwordx4 v[102:105], v[64:65], off offset:-112
	global_load_dwordx4 v[74:77], v[62:63], off offset:-96
	global_load_dwordx4 v[106:109], v[64:65], off offset:-96
	global_load_dwordx4 v[78:81], v[62:63], off offset:-80
	global_load_dwordx4 v[110:113], v[64:65], off offset:-80
	global_load_dwordx4 v[82:85], v[62:63], off
	global_load_dwordx4 v[114:117], v[64:65], off
	global_load_dwordx4 v[86:89], v[62:63], off offset:16
	global_load_dwordx4 v[118:121], v[64:65], off offset:16
	global_load_dwordx4 v[90:93], v[62:63], off offset:32
	global_load_dwordx4 v[122:125], v[64:65], off offset:32
	global_load_dwordx4 v[94:97], v[62:63], off offset:48
	global_load_dwordx4 v[126:129], v[64:65], off offset:48
	ds_read_b128 v[28:31], v27
	ds_read_b128 v[36:39], v27 offset:16
	ds_read_b128 v[40:43], v27 offset:8192
	ds_read_b128 v[50:53], v27 offset:8208
	ds_read_b128 v[130:133], v27 offset:32
	ds_read_b128 v[134:137], v27 offset:48
	ds_read_b128 v[138:141], v27 offset:8224
	ds_read_b128 v[142:145], v27 offset:8240
	s_waitcnt vmcnt(14) lgkmcnt(4)
	v_mul_f32_e32 v146, v18, v66
	v_mul_f32_e32 v147, v19, v67
	v_mul_f32_e32 v148, v20, v68
	v_mul_f32_e32 v149, v21, v69
	v_fma_f32 v146, v146, v28, v40
	v_fma_f32 v147, v147, v29, v41
	v_fma_f32 v148, v148, v30, v42
	v_fma_f32 v149, v149, v31, v43
	v_mfma_f32_32x32x2_f32 v[0:15], v146, v98, v[0:15]
	v_mfma_f32_32x32x2_f32 v[0:15], v147, v99, v[0:15]
	v_mfma_f32_32x32x2_f32 v[0:15], v148, v100, v[0:15]
	v_mfma_f32_32x32x2_f32 v[0:15], v149, v101, v[0:15]
	s_waitcnt vmcnt(12)
	v_mul_f32_e32 v146, v18, v70
	v_mul_f32_e32 v147, v19, v71
	v_mul_f32_e32 v148, v20, v72
	v_mul_f32_e32 v149, v21, v73
	v_fma_f32 v146, v146, v36, v50
	v_fma_f32 v147, v147, v37, v51
	v_fma_f32 v148, v148, v38, v52
	v_fma_f32 v149, v149, v39, v53
	v_mfma_f32_32x32x2_f32 v[0:15], v146, v102, v[0:15]
	v_mfma_f32_32x32x2_f32 v[0:15], v147, v103, v[0:15]
	v_mfma_f32_32x32x2_f32 v[0:15], v148, v104, v[0:15]
	v_mfma_f32_32x32x2_f32 v[0:15], v149, v105, v[0:15]
	ds_read_b128 v[28:31], v27 offset:128
	ds_read_b128 v[36:39], v27 offset:144
	ds_read_b128 v[40:43], v27 offset:8320
	ds_read_b128 v[50:53], v27 offset:8336
	s_waitcnt vmcnt(10) lgkmcnt(4)
	v_mul_f32_e32 v146, v18, v74
	v_mul_f32_e32 v147, v19, v75
	v_mul_f32_e32 v148, v20, v76
	v_mul_f32_e32 v149, v21, v77
	v_fma_f32 v146, v146, v130, v138
	v_fma_f32 v147, v147, v131, v139
	v_fma_f32 v148, v148, v132, v140
	v_fma_f32 v149, v149, v133, v141
	v_mfma_f32_32x32x2_f32 v[0:15], v146, v106, v[0:15]
	v_mfma_f32_32x32x2_f32 v[0:15], v147, v107, v[0:15]
	v_mfma_f32_32x32x2_f32 v[0:15], v148, v108, v[0:15]
	v_mfma_f32_32x32x2_f32 v[0:15], v149, v109, v[0:15]
	s_waitcnt vmcnt(8)
	v_mul_f32_e32 v146, v18, v78
	v_mul_f32_e32 v147, v19, v79
	v_mul_f32_e32 v148, v20, v80
	v_mul_f32_e32 v149, v21, v81
	v_fma_f32 v146, v146, v134, v142
	v_fma_f32 v147, v147, v135, v143
	v_fma_f32 v148, v148, v136, v144
	v_fma_f32 v149, v149, v137, v145
	v_mfma_f32_32x32x2_f32 v[0:15], v146, v110, v[0:15]
	v_mfma_f32_32x32x2_f32 v[0:15], v147, v111, v[0:15]
	v_mfma_f32_32x32x2_f32 v[0:15], v148, v112, v[0:15]
	v_mfma_f32_32x32x2_f32 v[0:15], v149, v113, v[0:15]
	ds_read_b128 v[130:133], v27 offset:160
	ds_read_b128 v[134:137], v27 offset:176
	ds_read_b128 v[138:141], v27 offset:8352
	ds_read_b128 v[142:145], v27 offset:8368
	s_waitcnt vmcnt(6) lgkmcnt(4)
	v_mul_f32_e32 v146, v18, v82
	v_mul_f32_e32 v147, v19, v83
	v_mul_f32_e32 v148, v20, v84
	v_mul_f32_e32 v149, v21, v85
	v_fma_f32 v146, v146, v28, v40
	v_fma_f32 v147, v147, v29, v41
	v_fma_f32 v148, v148, v30, v42
	v_fma_f32 v149, v149, v31, v43
	v_mfma_f32_32x32x2_f32 v[0:15], v146, v114, v[0:15]
	v_mfma_f32_32x32x2_f32 v[0:15], v147, v115, v[0:15]
	v_mfma_f32_32x32x2_f32 v[0:15], v148, v116, v[0:15]
	v_mfma_f32_32x32x2_f32 v[0:15], v149, v117, v[0:15]
	s_waitcnt vmcnt(4)
	v_mul_f32_e32 v146, v18, v86
	v_mul_f32_e32 v147, v19, v87
	v_mul_f32_e32 v148, v20, v88
	v_mul_f32_e32 v149, v21, v89
	v_fma_f32 v146, v146, v36, v50
	v_fma_f32 v147, v147, v37, v51
	v_fma_f32 v148, v148, v38, v52
	v_fma_f32 v149, v149, v39, v53
	v_mfma_f32_32x32x2_f32 v[0:15], v146, v118, v[0:15]
	v_mfma_f32_32x32x2_f32 v[0:15], v147, v119, v[0:15]
	v_mfma_f32_32x32x2_f32 v[0:15], v148, v120, v[0:15]
	v_mfma_f32_32x32x2_f32 v[0:15], v149, v121, v[0:15]
	s_waitcnt vmcnt(2) lgkmcnt(0)
	v_mul_f32_e32 v146, v18, v90
	v_mul_f32_e32 v147, v19, v91
	v_mul_f32_e32 v148, v20, v92
	v_mul_f32_e32 v149, v21, v93
	v_fma_f32 v146, v146, v130, v138
	v_fma_f32 v147, v147, v131, v139
	v_fma_f32 v148, v148, v132, v140
	v_fma_f32 v149, v149, v133, v141
	v_mfma_f32_32x32x2_f32 v[0:15], v146, v122, v[0:15]
	v_mfma_f32_32x32x2_f32 v[0:15], v147, v123, v[0:15]
	v_mfma_f32_32x32x2_f32 v[0:15], v148, v124, v[0:15]
	v_mfma_f32_32x32x2_f32 v[0:15], v149, v125, v[0:15]
	s_waitcnt vmcnt(0)
	v_mul_f32_e32 v146, v18, v94
	v_mul_f32_e32 v147, v19, v95
	v_mul_f32_e32 v148, v20, v96
	v_mul_f32_e32 v149, v21, v97
	v_fma_f32 v146, v146, v134, v142
	v_fma_f32 v147, v147, v135, v143
	v_fma_f32 v148, v148, v136, v144
	v_fma_f32 v149, v149, v137, v145
	v_mfma_f32_32x32x2_f32 v[0:15], v146, v126, v[0:15]
	v_mfma_f32_32x32x2_f32 v[0:15], v147, v127, v[0:15]
	v_mfma_f32_32x32x2_f32 v[0:15], v148, v128, v[0:15]
	v_mfma_f32_32x32x2_f32 v[0:15], v149, v129, v[0:15]
	v_add_u32_e32 v27, 0x100, v27
	s_add_u32 s2, s2, 0x100
	s_addc_u32 s3, s3, 0
	s_cmpk_eq_i32 s2, 0x400
	s_cbranch_scc0 .LBB0_938
	s_movk_i32 s3, 0x210
	s_mul_i32 s2, s82, 0x1080
	v_mul_lo_u32 v18, v26, s3
	v_add3_u32 v18, v16, v18, s2
	v_add_u32_e32 v19, 0x5000, v18
	s_nop 11
	ds_write2_b32 v19, v0, v1 offset1:33
	ds_write2_b32 v19, v2, v3 offset0:66 offset1:99
	v_add_u32_e32 v0, 0x5400, v18
	ds_write2_b32 v0, v4, v5 offset0:8 offset1:41
	ds_write2_b32 v0, v6, v7 offset0:74 offset1:107
	v_add_u32_e32 v0, 0x5800, v18
	s_movk_i32 s2, 0x400
	ds_write2_b32 v0, v8, v9 offset0:16 offset1:49
	ds_write2_b32 v0, v10, v11 offset0:82 offset1:115
	v_add_u32_e32 v0, 0x5c00, v18
	v_cmp_gt_i32_e32 vcc, s2, v32
	ds_write2_b32 v0, v12, v13 offset0:24 offset1:57
	ds_write2_b32 v0, v14, v15 offset0:90 offset1:123
	s_waitcnt lgkmcnt(0)
	s_barrier
	s_and_saveexec_b64 s[2:3], vcc
	s_cbranch_execz .LBB0_942
	v_lshlrev_b32_e32 v0, 2, v17
	global_load_dword v0, v0, s[12:13]
	s_mov_b64 s[6:7], 0
	s_movk_i32 s4, 0x84
	s_movk_i32 s5, 0x1ff
	v_mov_b32_e32 v1, v32
